# mixer-B softmax section: K/V LDS writes grouped at the end of the section (after the converts)
# speedup vs baseline: 1.0252x; 1.0220x over previous
; #define ATT_SBAR() __builtin_amdgcn_sched_barrier(0)
; #define ATT_PK4(P, BASE, OUT) do { u32x4 w = {cvtpk(P[BASE + 0], P[BASE + 1]), cvtpk(P[BASE + 2], P[BASE + 3]), cvtpk(P[BASE + 4], P[BASE + 5]), cvtpk(P[BASE + 6], P[BASE + 7])}; \
;     OUT = *reinterpret_cast<bf16x8*>(&w); } while (0)
; #define ATT_WRITE_K(so) do { *(bf16x8*)(K_lds + (so) + kswz<DQK>(kr, kc * 2)) = sk0; if constexpr (DQK == 128) *(bf16x8*)(K_lds + (so) + kswz<DQK>(32 + kr, kc * 2)) = sk1; } while (0)
; #define ATT_WRITE_V(so) do { *(bf16x8*)(V_lds + (so) + vst0) = sv0; *(bf16x8*)(V_lds + (so) + vst1) = sv1; } while (0)
; #define ATT_BAR() do { ATT_SBAR(); asm volatile("s_barrier" ::: "memory"); ATT_SBAR(); } while (0)
; #define ATT_VPAIR(buf, so, blk, ks) do { if constexpr (!(ABL & 8) && !(ABL & 32)) { buf[2 * (ks)] = vtr(vq0 + (so) + v_rd_off(blk, ks, 0)); buf[2 * (ks) + 1] = vtr(vq0 + (so) + v_rd_off(blk, ks, 1)); } } while (0)
; __device__ __forceinline__ void softmax_exp_pack(f32x16& p0, f32x16& p1, bf16x8& pa0, bf16x8& pa1, bf16x8& pa2, bf16x8& pa3) {
; #pragma unroll
;   for (int r = 0; r < 16; ++r) { p0[r] = __builtin_amdgcn_exp2f(p0[r]); p1[r] = __builtin_amdgcn_exp2f(p1[r]); }
;     ...
;   ATT_PK4(p0, 0, pa0); ATT_PK4(p0, 8, pa1); ATT_PK4(p1, 0, pa2); ATT_PK4(p1, 8, pa3);
;     ...
;     if constexpr (!(ABL & 4)) { ATT_WRITE_K(k2); ATT_WRITE_V(v1); }
;     ATT_SBAR();
; #pragma unroll
;     for (int ks = 0; ks < 4; ++ks) ATT_VPAIR(va, v0, 0, ks);
;     asm volatile("s_waitcnt lgkmcnt(8)" ::: "memory"); ATT_BAR();
.LBB0_283:
	v_exp_f32_e32 v98, v98
	v_exp_f32_e32 v114, v114
	v_exp_f32_e32 v99, v99
	v_exp_f32_e32 v115, v115
	v_exp_f32_e32 v100, v100
	v_exp_f32_e32 v101, v101
	v_exp_f32_e32 v102, v102
	v_exp_f32_e32 v103, v103
	v_exp_f32_e32 v106, v106
	v_exp_f32_e32 v107, v107
	v_exp_f32_e32 v116, v116
	v_exp_f32_e32 v117, v117
	v_exp_f32_e32 v118, v118
	v_exp_f32_e32 v119, v119
	v_exp_f32_e32 v104, v104
	v_exp_f32_e32 v120, v120
	v_exp_f32_e32 v105, v105
	v_exp_f32_e32 v121, v121
	v_exp_f32_e32 v122, v122
	v_exp_f32_e32 v123, v123
	v_exp_f32_e32 v108, v108
	v_exp_f32_e32 v124, v124
	v_exp_f32_e32 v109, v109
	v_exp_f32_e32 v125, v125
	v_exp_f32_e32 v110, v110
	v_exp_f32_e32 v126, v126
	v_exp_f32_e32 v111, v111
	v_exp_f32_e32 v127, v127
	v_exp_f32_e32 v112, v112
	v_exp_f32_e32 v128, v128
	v_exp_f32_e32 v113, v113
	v_exp_f32_e32 v129, v129
	v_cvt_pk_bf16_f32 v2, v98, v99
	v_cvt_pk_bf16_f32 v3, v100, v101
	v_cvt_pk_bf16_f32 v4, v102, v103
	v_cvt_pk_bf16_f32 v6, v106, v107
	v_cvt_pk_bf16_f32 v10, v114, v115
	v_cvt_pk_bf16_f32 v5, v104, v105
	v_cvt_pk_bf16_f32 v7, v108, v109
	v_cvt_pk_bf16_f32 v8, v110, v111
	v_cvt_pk_bf16_f32 v9, v112, v113
	v_cvt_pk_bf16_f32 v11, v116, v117
	v_cvt_pk_bf16_f32 v12, v118, v119
	v_cvt_pk_bf16_f32 v13, v120, v121
	v_cvt_pk_bf16_f32 v14, v122, v123
	v_cvt_pk_bf16_f32 v15, v124, v125
	v_cvt_pk_bf16_f32 v16, v126, v127
	v_cvt_pk_bf16_f32 v17, v128, v129
	s_waitcnt vmcnt(0)
	v_add_u32_e32 v114, s94, v169
	ds_write_b128 v114, v[224:227] offset:49152
	v_add_u32_e32 v114, s95, v167
	ds_write_b128 v114, v[228:231]
	v_add_u32_e32 v114, s95, v168
	ds_write_b128 v114, v[232:235]
	v_add_u32_e32 v249, s96, v172
	ds_read_b128 v[152:155], v249 offset:49152
	ds_read_b128 v[156:159], v249 offset:53760
	ds_read_b128 v[160:163], v249 offset:49184
	ds_read_b128 v[176:179], v249 offset:53792
	s_waitcnt lgkmcnt(4)
	s_barrier
; #define ATT_SBAR() __builtin_amdgcn_sched_barrier(0)
; __device__ __forceinline__ float softmax_rowmax(const f32x16& p0, const f32x16& p1) {
;   const float m0 = p1[0] + 0.0f; float a, b;
;   asm("v_max3_f32 %0, %1, %2, %3\n\tv_max3_f32 %0, %0, %4, %5\n\tv_max3_f32 %0, %0, %6, %7\n\tv_max3_f32 %0, %0, %8, %9\n\t"
;       "v_max3_f32 %0, %0, %10, %11\n\tv_max3_f32 %0, %0, %12, %13\n\tv_max3_f32 %0, %0, %14, %15\n\tv_max3_f32 %0, %0, %16, %17"
;       : "=&v"(a) : "v"(m0), "v"(p0[0]), "v"(p0[1]), "v"(p0[2]), "v"(p0[3]), "v"(p0[4]), "v"(p0[5]), "v"(p0[6]), "v"(p0[7]), "v"(p0[8]), "v"(p0[9]), "v"(p0[10]), "v"(p0[11]), "v"(p0[12]), "v"(p0[13]), "v"(p0[14]), "v"(p0[15]));
;   asm("v_max3_f32 %0, %1, %2, %3\n\tv_max3_f32 %0, %0, %4, %5\n\tv_max3_f32 %0, %0, %6, %7\n\tv_max3_f32 %0, %0, %8, %9\n\t"
;       "v_max3_f32 %0, %0, %10, %11\n\tv_max3_f32 %0, %0, %12, %13\n\tv_max3_f32 %0, %0, %14, %15\n\tv_max_f32 %0, %0, %16"
;       : "=&v"(b) : "v"(a), "v"(p1[1]), "v"(p1[2]), "v"(p1[3]), "v"(p1[4]), "v"(p1[5]), "v"(p1[6]), "v"(p1[7]), "v"(p1[8]), "v"(p1[9]), "v"(p1[10]), "v"(p1[11]), "v"(p1[12]), "v"(p1[13]), "v"(p1[14]), "v"(p1[15]));
;   return b;
;     ...
;   for (int t = 0; t + 1 < NT; ++t) {
;     if constexpr (ABL & 1) { u32x4 w0 = {cvtpk(p0[0], p0[1]), cvtpk(p0[2], p0[3]), cvtpk(p0[4], p0[5]), cvtpk(p0[6], p0[7])}, w1 = {cvtpk(p0[8], p0[9]), cvtpk(p0[10], p0[11]), cvtpk(p0[12], p0[13]), cvtpk(p0[14], p0[15])};
;         u32x4 w2 = {cvtpk(p1[0], p1[1]), cvtpk(p1[2], p1[3]), cvtpk(p1[4], p1[5]), cvtpk(p1[6], p1[7])}, w3 = {cvtpk(p1[8], p1[9]), cvtpk(p1[10], p1[11]), cvtpk(p1[12], p1[13]), cvtpk(p1[14], p1[15])};
;         pa0 = *reinterpret_cast<bf16x8*>(&w0); pa1 = *reinterpret_cast<bf16x8*>(&w1); pa2 = *reinterpret_cast<bf16x8*>(&w2); pa3 = *reinterpret_cast<bf16x8*>(&w3); }
;     else { ATT_SOFTMAX(t == 0); }
;     if constexpr (!(ABL & 4)) { ATT_WRITE_K(k2); ATT_WRITE_V(v1); }
;     ATT_SBAR();
; #pragma unroll
;     for (int ks = 0; ks < 4; ++ks) ATT_VPAIR(va, v0, 0, ks);
;     asm volatile("s_waitcnt lgkmcnt(8)" ::: "memory"); ATT_BAR();
;     ATT_XSECTION(true);
;     if constexpr (!(ABL & 4)) { const int tk = (t + 3 < NT) ? t + 3 : NT - 1, tv = (t + 2 < NT) ? t + 2 : NT - 1; ATT_LOAD_K(tk); ATT_LOAD_V(tv); }
;     ATT_BAR();
;     { const int tk_ = k0; k0 = k1; k1 = k2; k2 = tk_; const int tv_ = v0; v0 = v1; v1 = v2; v2 = tv_; }
	s_setprio 2
	s_waitcnt lgkmcnt(3)
	v_mfma_f32_32x32x16_bf16 v[98:113], v[152:155], v[136:139], v[82:97]
	ds_read_b128 v[180:183], v249 offset:49216
	s_waitcnt lgkmcnt(3)
	v_mfma_f32_32x32x16_bf16 v[114:129], v[156:159], v[136:139], v[82:97]
	ds_read_b128 v[186:189], v249 offset:53824
	v_add_u32_e32 v248, s37, v131
	s_waitcnt lgkmcnt(3)
	v_mfma_f32_32x32x16_bf16 v[98:113], v[160:163], v[140:143], v[98:113]
	ds_read_b128 v[190:193], v249 offset:49248
	ds_read_b64_tr_b16 v[198:199], v248
	ds_read_b64_tr_b16 v[200:201], v248 offset:2048
	s_waitcnt lgkmcnt(5)
	v_mfma_f32_32x32x16_bf16 v[114:129], v[176:179], v[140:143], v[114:129]
	ds_read_b128 v[194:197], v249 offset:53856
	ds_read_b64_tr_b16 v[212:213], v248 offset:4096
	ds_read_b64_tr_b16 v[214:215], v248 offset:6144
	s_waitcnt lgkmcnt(7)
	v_mfma_f32_32x32x16_bf16 v[98:113], v[180:183], v[144:147], v[98:113]
	ds_read_b64_tr_b16 v[216:217], v248 offset:8192
	ds_read_b64_tr_b16 v[218:219], v248 offset:10240
	s_waitcnt lgkmcnt(8)
	v_mfma_f32_32x32x16_bf16 v[114:129], v[186:189], v[144:147], v[114:129]
	ds_read_b64_tr_b16 v[220:221], v248 offset:12288
	ds_read_b64_tr_b16 v[222:223], v248 offset:14336
	s_waitcnt lgkmcnt(9)
	v_mfma_f32_32x32x16_bf16 v[98:113], v[190:193], v[148:151], v[98:113]
	s_waitcnt lgkmcnt(6)
	v_mfma_f32_32x32x16_bf16 v[114:129], v[194:197], v[148:151], v[114:129]
	v_mfma_f32_32x32x16_bf16 v[18:33], v[2:5], v[198:201], v[18:33]
	ds_read_b64_tr_b16 v[236:237], v248 offset:512
	ds_read_b64_tr_b16 v[238:239], v248 offset:2560
	s_waitcnt lgkmcnt(6)
	v_mfma_f32_32x32x16_bf16 v[18:33], v[6:9], v[212:215], v[18:33]
	ds_read_b64_tr_b16 v[198:199], v248 offset:4608
	ds_read_b64_tr_b16 v[200:201], v248 offset:6656
	s_waitcnt lgkmcnt(6)
	v_mfma_f32_32x32x16_bf16 v[18:33], v[10:13], v[216:219], v[18:33]
	ds_read_b64_tr_b16 v[212:213], v248 offset:8704
	ds_read_b64_tr_b16 v[214:215], v248 offset:10752
	s_waitcnt lgkmcnt(6)
	v_mfma_f32_32x32x16_bf16 v[18:33], v[14:17], v[220:223], v[18:33]
	ds_read_b64_tr_b16 v[216:217], v248 offset:12800
	ds_read_b64_tr_b16 v[218:219], v248 offset:14848
	v_max3_f32 v249, v98, v99, v100
	s_waitcnt lgkmcnt(6)
	v_mfma_f32_32x32x16_bf16 v[34:49], v[2:5], v[236:239], v[34:49]
	ds_read_b64_tr_b16 v[220:221], v248 offset:1024
	ds_read_b64_tr_b16 v[222:223], v248 offset:3072
	v_max3_f32 v173, v114, v115, v116
	s_waitcnt lgkmcnt(6)
	v_mfma_f32_32x32x16_bf16 v[34:49], v[6:9], v[198:201], v[34:49]
	ds_read_b64_tr_b16 v[236:237], v248 offset:5120
	ds_read_b64_tr_b16 v[238:239], v248 offset:7168
	v_max3_f32 v249, v249, v101, v102
	s_waitcnt lgkmcnt(6)
	v_mfma_f32_32x32x16_bf16 v[34:49], v[10:13], v[212:215], v[34:49]
	ds_read_b64_tr_b16 v[198:199], v248 offset:9216
	ds_read_b64_tr_b16 v[200:201], v248 offset:11264
	v_max3_f32 v173, v173, v117, v118
	s_waitcnt lgkmcnt(6)
	v_mfma_f32_32x32x16_bf16 v[34:49], v[14:17], v[216:219], v[34:49]
	ds_read_b64_tr_b16 v[212:213], v248 offset:13312
	ds_read_b64_tr_b16 v[214:215], v248 offset:15360
	v_max3_f32 v249, v249, v103, v104
	s_waitcnt lgkmcnt(6)
	v_mfma_f32_32x32x16_bf16 v[50:65], v[2:5], v[220:223], v[50:65]
	ds_read_b64_tr_b16 v[216:217], v248 offset:1536
	ds_read_b64_tr_b16 v[218:219], v248 offset:3584
	v_max3_f32 v173, v173, v119, v120
	s_waitcnt lgkmcnt(6)
	v_mfma_f32_32x32x16_bf16 v[50:65], v[6:9], v[236:239], v[50:65]
	ds_read_b64_tr_b16 v[220:221], v248 offset:5632
	ds_read_b64_tr_b16 v[222:223], v248 offset:7680
	v_max3_f32 v249, v249, v105, v106
	s_waitcnt lgkmcnt(6)
	v_mfma_f32_32x32x16_bf16 v[50:65], v[10:13], v[198:201], v[50:65]
	ds_read_b64_tr_b16 v[236:237], v248 offset:9728
	ds_read_b64_tr_b16 v[238:239], v248 offset:11776
	v_max3_f32 v173, v173, v121, v122
	s_waitcnt lgkmcnt(6)
	v_mfma_f32_32x32x16_bf16 v[50:65], v[14:17], v[212:215], v[50:65]
	ds_read_b64_tr_b16 v[198:199], v248 offset:13824
	ds_read_b64_tr_b16 v[200:201], v248 offset:15872
	v_max3_f32 v249, v249, v107, v108
	s_waitcnt lgkmcnt(6)
	v_mfma_f32_32x32x16_bf16 v[66:81], v[2:5], v[216:219], v[66:81]
	v_max3_f32 v173, v173, v123, v124
	s_min_u32 s14, s97, 0x7c
	s_lshl_b32 s14, s14, 17
	s_add_i32 s14, s14, 0x60000
	buffer_load_dwordx4 v[224:227], v170, s[8:11], s14 offen
	s_waitcnt lgkmcnt(4)
	v_mfma_f32_32x32x16_bf16 v[66:81], v[6:9], v[220:223], v[66:81]
	v_max3_f32 v249, v249, v109, v110
	s_add_i32 s19, s36, 0xffff0000
	s_mov_b32 s14, s10
	s_mov_b32 s15, s11
	buffer_load_dwordx4 v[228:231], v171, s[12:15], s19 offen
	s_waitcnt lgkmcnt(2)
	v_mfma_f32_32x32x16_bf16 v[66:81], v[10:13], v[236:239], v[66:81]
	v_max3_f32 v173, v173, v125, v126
	buffer_load_dwordx4 v[232:235], v171, s[12:15], s36 offen
	s_waitcnt lgkmcnt(0)
	v_mfma_f32_32x32x16_bf16 v[66:81], v[14:17], v[198:201], v[66:81]
	v_max3_f32 v249, v249, v111, v112
	v_mfma_f32_4x4x4_16b_bf16 v[240:243], v[2:3], v[132:133], v[240:243]
	v_max3_f32 v173, v173, v127, v128
	v_mfma_f32_4x4x4_16b_bf16 v[244:247], v[4:5], v[132:133], v[244:247]
	v_mfma_f32_4x4x4_16b_bf16 v[240:243], v[6:7], v[132:133], v[240:243]
	v_max_f32 v249, v249, v113
	v_mfma_f32_4x4x4_16b_bf16 v[244:247], v[8:9], v[132:133], v[244:247]
	v_mfma_f32_4x4x4_16b_bf16 v[240:243], v[10:11], v[132:133], v[240:243]
	v_max_f32 v173, v173, v129
	v_mfma_f32_4x4x4_16b_bf16 v[244:247], v[12:13], v[132:133], v[244:247]
	v_mfma_f32_4x4x4_16b_bf16 v[240:243], v[14:15], v[132:133], v[240:243]
	v_max_f32 v173, v173, v249
	v_mfma_f32_4x4x4_16b_bf16 v[244:247], v[16:17], v[132:133], v[244:247]
	s_setprio 0
	s_barrier
	s_add_i32 s36, s36, 0x20000
	s_add_i32 s97, s97, 1
	s_cmpk_eq_i32 s97, 0x7e
	s_cbranch_scc1 .LBB0_290
	s_mov_b32 s14, s94
	s_mov_b32 s94, s18
	s_mov_b32 s18, s96
	s_mov_b32 s15, s95
	s_mov_b32 s95, s93
	s_mov_b32 s93, s37
	s_branch .LBB0_282

; #define ATT_SBAR() __builtin_amdgcn_sched_barrier(0)
; #define ATT_PK4(P, BASE, OUT) do { u32x4 w = {cvtpk(P[BASE + 0], P[BASE + 1]), cvtpk(P[BASE + 2], P[BASE + 3]), cvtpk(P[BASE + 4], P[BASE + 5]), cvtpk(P[BASE + 6], P[BASE + 7])}; \
;     OUT = *reinterpret_cast<bf16x8*>(&w); } while (0)
; #define ATT_WRITE_K(so) do { *(bf16x8*)(K_lds + (so) + kswz<DQK>(kr, kc * 2)) = sk0; if constexpr (DQK == 128) *(bf16x8*)(K_lds + (so) + kswz<DQK>(32 + kr, kc * 2)) = sk1; } while (0)
; #define ATT_WRITE_V(so) do { *(bf16x8*)(V_lds + (so) + vst0) = sv0; *(bf16x8*)(V_lds + (so) + vst1) = sv1; } while (0)
; #define ATT_BAR() do { ATT_SBAR(); asm volatile("s_barrier" ::: "memory"); ATT_SBAR(); } while (0)
; #define ATT_VPAIR(buf, so, blk, ks) do { if constexpr (!(ABL & 8) && !(ABL & 32)) { buf[2 * (ks)] = vtr(vq0 + (so) + v_rd_off(blk, ks, 0)); buf[2 * (ks) + 1] = vtr(vq0 + (so) + v_rd_off(blk, ks, 1)); } } while (0)
; __device__ __forceinline__ void softmax_exp_pack(f32x16& p0, f32x16& p1, bf16x8& pa0, bf16x8& pa1, bf16x8& pa2, bf16x8& pa3) {
; #pragma unroll
;   for (int r = 0; r < 16; ++r) { p0[r] = __builtin_amdgcn_exp2f(p0[r]); p1[r] = __builtin_amdgcn_exp2f(p1[r]); }
;     ...
;   ATT_PK4(p0, 0, pa0); ATT_PK4(p0, 8, pa1); ATT_PK4(p1, 0, pa2); ATT_PK4(p1, 8, pa3);
;     ...
;     if constexpr (!(ABL & 4)) { ATT_WRITE_K(k2); ATT_WRITE_V(v1); }
;     ATT_SBAR();
; #pragma unroll
;     for (int ks = 0; ks < 4; ++ks) ATT_VPAIR(va, v0, 0, ks);
;     asm volatile("s_waitcnt lgkmcnt(8)" ::: "memory"); ATT_BAR();
.LBB0_298:
	v_exp_f32_e32 v98, v98
	v_exp_f32_e32 v114, v114
	v_exp_f32_e32 v99, v99
	v_exp_f32_e32 v115, v115
	v_exp_f32_e32 v100, v100
	v_exp_f32_e32 v101, v101
	v_exp_f32_e32 v102, v102
	v_exp_f32_e32 v103, v103
	v_exp_f32_e32 v106, v106
	v_exp_f32_e32 v107, v107
	v_exp_f32_e32 v116, v116
	v_exp_f32_e32 v117, v117
	v_exp_f32_e32 v118, v118
	v_exp_f32_e32 v119, v119
	v_exp_f32_e32 v104, v104
	v_exp_f32_e32 v120, v120
	v_exp_f32_e32 v105, v105
	v_exp_f32_e32 v121, v121
	v_exp_f32_e32 v122, v122
	v_exp_f32_e32 v123, v123
	v_exp_f32_e32 v108, v108
	v_exp_f32_e32 v124, v124
	v_exp_f32_e32 v109, v109
	v_exp_f32_e32 v125, v125
	v_exp_f32_e32 v110, v110
	v_exp_f32_e32 v126, v126
	v_exp_f32_e32 v111, v111
	v_exp_f32_e32 v127, v127
	v_exp_f32_e32 v112, v112
	v_exp_f32_e32 v128, v128
	v_exp_f32_e32 v113, v113
	v_exp_f32_e32 v129, v129
	v_cvt_pk_bf16_f32 v18, v98, v99
	v_cvt_pk_bf16_f32 v19, v100, v101
	v_cvt_pk_bf16_f32 v20, v102, v103
	v_cvt_pk_bf16_f32 v22, v106, v107
	v_cvt_pk_bf16_f32 v26, v114, v115
	v_cvt_pk_bf16_f32 v21, v104, v105
	v_cvt_pk_bf16_f32 v23, v108, v109
	v_cvt_pk_bf16_f32 v24, v110, v111
	v_cvt_pk_bf16_f32 v25, v112, v113
	v_cvt_pk_bf16_f32 v27, v116, v117
	v_cvt_pk_bf16_f32 v28, v118, v119
	v_cvt_pk_bf16_f32 v29, v120, v121
	v_cvt_pk_bf16_f32 v30, v122, v123
	v_cvt_pk_bf16_f32 v31, v124, v125
	v_cvt_pk_bf16_f32 v32, v126, v127
	v_cvt_pk_bf16_f32 v33, v128, v129
	s_waitcnt vmcnt(0)
	v_add_u32_e32 v114, s49, v170
	ds_write_b128 v114, v[224:227] offset:49152
	v_add_u32_e32 v114, s50, v168
	ds_write_b128 v114, v[228:231]
	v_add_u32_e32 v114, s50, v169
	ds_write_b128 v114, v[232:235]
	v_add_u32_e32 v249, s18, v173
	ds_read_b128 v[152:155], v249 offset:49152
	ds_read_b128 v[156:159], v249 offset:53760
	ds_read_b128 v[160:163], v249 offset:49184
	ds_read_b128 v[176:179], v249 offset:53792
	s_waitcnt lgkmcnt(4)
	s_barrier
; #define ATT_SBAR() __builtin_amdgcn_sched_barrier(0)
; __device__ __forceinline__ float softmax_rowmax(const f32x16& p0, const f32x16& p1) {
;   const float m0 = p1[0] + 0.0f; float a, b;
;   asm("v_max3_f32 %0, %1, %2, %3\n\tv_max3_f32 %0, %0, %4, %5\n\tv_max3_f32 %0, %0, %6, %7\n\tv_max3_f32 %0, %0, %8, %9\n\t"
;       "v_max3_f32 %0, %0, %10, %11\n\tv_max3_f32 %0, %0, %12, %13\n\tv_max3_f32 %0, %0, %14, %15\n\tv_max3_f32 %0, %0, %16, %17"
;       : "=&v"(a) : "v"(m0), "v"(p0[0]), "v"(p0[1]), "v"(p0[2]), "v"(p0[3]), "v"(p0[4]), "v"(p0[5]), "v"(p0[6]), "v"(p0[7]), "v"(p0[8]), "v"(p0[9]), "v"(p0[10]), "v"(p0[11]), "v"(p0[12]), "v"(p0[13]), "v"(p0[14]), "v"(p0[15]));
;   asm("v_max3_f32 %0, %1, %2, %3\n\tv_max3_f32 %0, %0, %4, %5\n\tv_max3_f32 %0, %0, %6, %7\n\tv_max3_f32 %0, %0, %8, %9\n\t"
;       "v_max3_f32 %0, %0, %10, %11\n\tv_max3_f32 %0, %0, %12, %13\n\tv_max3_f32 %0, %0, %14, %15\n\tv_max_f32 %0, %0, %16"
;       : "=&v"(b) : "v"(a), "v"(p1[1]), "v"(p1[2]), "v"(p1[3]), "v"(p1[4]), "v"(p1[5]), "v"(p1[6]), "v"(p1[7]), "v"(p1[8]), "v"(p1[9]), "v"(p1[10]), "v"(p1[11]), "v"(p1[12]), "v"(p1[13]), "v"(p1[14]), "v"(p1[15]));
;   return b;
;     ...
;   for (int t = 0; t + 1 < NT; ++t) {
;     if constexpr (ABL & 1) { u32x4 w0 = {cvtpk(p0[0], p0[1]), cvtpk(p0[2], p0[3]), cvtpk(p0[4], p0[5]), cvtpk(p0[6], p0[7])}, w1 = {cvtpk(p0[8], p0[9]), cvtpk(p0[10], p0[11]), cvtpk(p0[12], p0[13]), cvtpk(p0[14], p0[15])};
;         u32x4 w2 = {cvtpk(p1[0], p1[1]), cvtpk(p1[2], p1[3]), cvtpk(p1[4], p1[5]), cvtpk(p1[6], p1[7])}, w3 = {cvtpk(p1[8], p1[9]), cvtpk(p1[10], p1[11]), cvtpk(p1[12], p1[13]), cvtpk(p1[14], p1[15])};
;         pa0 = *reinterpret_cast<bf16x8*>(&w0); pa1 = *reinterpret_cast<bf16x8*>(&w1); pa2 = *reinterpret_cast<bf16x8*>(&w2); pa3 = *reinterpret_cast<bf16x8*>(&w3); }
;     else { ATT_SOFTMAX(t == 0); }
;     if constexpr (!(ABL & 4)) { ATT_WRITE_K(k2); ATT_WRITE_V(v1); }
;     ATT_SBAR();
; #pragma unroll
;     for (int ks = 0; ks < 4; ++ks) ATT_VPAIR(va, v0, 0, ks);
;     asm volatile("s_waitcnt lgkmcnt(8)" ::: "memory"); ATT_BAR();
;     ATT_XSECTION(true);
;     if constexpr (!(ABL & 4)) { const int tk = (t + 3 < NT) ? t + 3 : NT - 1, tv = (t + 2 < NT) ? t + 2 : NT - 1; ATT_LOAD_K(tk); ATT_LOAD_V(tv); }
;     ATT_BAR();
;     { const int tk_ = k0; k0 = k1; k1 = k2; k2 = tk_; const int tv_ = v0; v0 = v1; v1 = v2; v2 = tv_; }
	s_setprio 2
	s_waitcnt lgkmcnt(3)
	v_mfma_f32_32x32x16_bf16 v[98:113], v[152:155], v[136:139], v[82:97]
	ds_read_b128 v[180:183], v249 offset:49216
	s_waitcnt lgkmcnt(3)
	v_mfma_f32_32x32x16_bf16 v[114:129], v[156:159], v[136:139], v[82:97]
	ds_read_b128 v[186:189], v249 offset:53824
	v_add_u32_e32 v248, s37, v131
	s_waitcnt lgkmcnt(3)
	v_mfma_f32_32x32x16_bf16 v[98:113], v[160:163], v[140:143], v[98:113]
	ds_read_b128 v[190:193], v249 offset:49248
	ds_read_b64_tr_b16 v[198:199], v248
	ds_read_b64_tr_b16 v[200:201], v248 offset:2048
	s_waitcnt lgkmcnt(5)
	v_mfma_f32_32x32x16_bf16 v[114:129], v[176:179], v[140:143], v[114:129]
	ds_read_b128 v[194:197], v249 offset:53856
	ds_read_b64_tr_b16 v[212:213], v248 offset:4096
	ds_read_b64_tr_b16 v[214:215], v248 offset:6144
	s_waitcnt lgkmcnt(7)
	v_mfma_f32_32x32x16_bf16 v[98:113], v[180:183], v[144:147], v[98:113]
	ds_read_b64_tr_b16 v[216:217], v248 offset:8192
	ds_read_b64_tr_b16 v[218:219], v248 offset:10240
	s_waitcnt lgkmcnt(8)
	v_mfma_f32_32x32x16_bf16 v[114:129], v[186:189], v[144:147], v[114:129]
	ds_read_b64_tr_b16 v[220:221], v248 offset:12288
	ds_read_b64_tr_b16 v[222:223], v248 offset:14336
	s_waitcnt lgkmcnt(9)
	v_mfma_f32_32x32x16_bf16 v[98:113], v[190:193], v[148:151], v[98:113]
	s_waitcnt lgkmcnt(6)
	v_mfma_f32_32x32x16_bf16 v[114:129], v[194:197], v[148:151], v[114:129]
	v_mfma_f32_32x32x16_bf16 v[66:81], v[18:21], v[198:201], v[66:81]
	ds_read_b64_tr_b16 v[236:237], v248 offset:512
	ds_read_b64_tr_b16 v[238:239], v248 offset:2560
	s_waitcnt lgkmcnt(6)
	v_mfma_f32_32x32x16_bf16 v[66:81], v[22:25], v[212:215], v[66:81]
	ds_read_b64_tr_b16 v[198:199], v248 offset:4608
	ds_read_b64_tr_b16 v[200:201], v248 offset:6656
	s_waitcnt lgkmcnt(6)
	v_mfma_f32_32x32x16_bf16 v[66:81], v[26:29], v[216:219], v[66:81]
	ds_read_b64_tr_b16 v[212:213], v248 offset:8704
	ds_read_b64_tr_b16 v[214:215], v248 offset:10752
	s_waitcnt lgkmcnt(6)
	v_mfma_f32_32x32x16_bf16 v[66:81], v[30:33], v[220:223], v[66:81]
	ds_read_b64_tr_b16 v[216:217], v248 offset:12800
	ds_read_b64_tr_b16 v[218:219], v248 offset:14848
	v_max3_f32 v249, v98, v99, v100
	s_waitcnt lgkmcnt(6)
	v_mfma_f32_32x32x16_bf16 v[50:65], v[18:21], v[236:239], v[50:65]
	ds_read_b64_tr_b16 v[220:221], v248 offset:1024
	ds_read_b64_tr_b16 v[222:223], v248 offset:3072
	v_max3_f32 v174, v114, v115, v116
	s_waitcnt lgkmcnt(6)
	v_mfma_f32_32x32x16_bf16 v[50:65], v[22:25], v[198:201], v[50:65]
	ds_read_b64_tr_b16 v[236:237], v248 offset:5120
	ds_read_b64_tr_b16 v[238:239], v248 offset:7168
	v_max3_f32 v249, v249, v101, v102
	s_waitcnt lgkmcnt(6)
	v_mfma_f32_32x32x16_bf16 v[50:65], v[26:29], v[212:215], v[50:65]
	ds_read_b64_tr_b16 v[198:199], v248 offset:9216
	ds_read_b64_tr_b16 v[200:201], v248 offset:11264
	v_max3_f32 v174, v174, v117, v118
	s_waitcnt lgkmcnt(6)
	v_mfma_f32_32x32x16_bf16 v[50:65], v[30:33], v[216:219], v[50:65]
	ds_read_b64_tr_b16 v[212:213], v248 offset:13312
	ds_read_b64_tr_b16 v[214:215], v248 offset:15360
	v_max3_f32 v249, v249, v103, v104
	s_waitcnt lgkmcnt(6)
	v_mfma_f32_32x32x16_bf16 v[34:49], v[18:21], v[220:223], v[34:49]
	ds_read_b64_tr_b16 v[216:217], v248 offset:1536
	ds_read_b64_tr_b16 v[218:219], v248 offset:3584
	v_max3_f32 v174, v174, v119, v120
	s_waitcnt lgkmcnt(6)
	v_mfma_f32_32x32x16_bf16 v[34:49], v[22:25], v[236:239], v[34:49]
	ds_read_b64_tr_b16 v[220:221], v248 offset:5632
	ds_read_b64_tr_b16 v[222:223], v248 offset:7680
	v_max3_f32 v249, v249, v105, v106
	s_waitcnt lgkmcnt(6)
	v_mfma_f32_32x32x16_bf16 v[34:49], v[26:29], v[198:201], v[34:49]
	ds_read_b64_tr_b16 v[236:237], v248 offset:9728
	ds_read_b64_tr_b16 v[238:239], v248 offset:11776
	v_max3_f32 v174, v174, v121, v122
	s_waitcnt lgkmcnt(6)
	v_mfma_f32_32x32x16_bf16 v[34:49], v[30:33], v[212:215], v[34:49]
	ds_read_b64_tr_b16 v[198:199], v248 offset:13824
	ds_read_b64_tr_b16 v[200:201], v248 offset:15872
	v_max3_f32 v249, v249, v107, v108
	s_waitcnt lgkmcnt(6)
	v_mfma_f32_32x32x16_bf16 v[2:17], v[18:21], v[216:219], v[2:17]
	v_max3_f32 v174, v174, v123, v124
	s_min_u32 s14, s90, 0x7c
	s_lshl_b32 s14, s14, 17
	s_add_i32 s19, s14, 0x60000
	s_add_i32 s92, s36, 0xffff0000
	s_mov_b32 s14, s10
	s_mov_b32 s15, s11
	buffer_load_dwordx4 v[224:227], v171, s[8:11], s19 offen
	s_waitcnt lgkmcnt(4)
	v_mfma_f32_32x32x16_bf16 v[2:17], v[22:25], v[220:223], v[2:17]
	v_max3_f32 v249, v249, v109, v110
	buffer_load_dwordx4 v[228:231], v172, s[12:15], s92 offen
	s_waitcnt lgkmcnt(2)
	v_mfma_f32_32x32x16_bf16 v[2:17], v[26:29], v[236:239], v[2:17]
	v_max3_f32 v174, v174, v125, v126
	buffer_load_dwordx4 v[232:235], v172, s[12:15], s36 offen
	s_waitcnt lgkmcnt(0)
	v_mfma_f32_32x32x16_bf16 v[2:17], v[30:33], v[198:201], v[2:17]
	v_max3_f32 v249, v249, v111, v112
	v_mfma_f32_4x4x4_16b_bf16 v[240:243], v[18:19], v[132:133], v[240:243]
	v_max3_f32 v174, v174, v127, v128
	v_mfma_f32_4x4x4_16b_bf16 v[244:247], v[20:21], v[132:133], v[244:247]
	v_mfma_f32_4x4x4_16b_bf16 v[240:243], v[22:23], v[132:133], v[240:243]
	v_max_f32 v249, v249, v113
	v_mfma_f32_4x4x4_16b_bf16 v[244:247], v[24:25], v[132:133], v[244:247]
	v_mfma_f32_4x4x4_16b_bf16 v[240:243], v[26:27], v[132:133], v[240:243]
	v_max_f32 v174, v174, v129
	v_mfma_f32_4x4x4_16b_bf16 v[244:247], v[28:29], v[132:133], v[244:247]
	v_mfma_f32_4x4x4_16b_bf16 v[240:243], v[30:31], v[132:133], v[240:243]
	v_max_f32 v174, v174, v249
	v_mfma_f32_4x4x4_16b_bf16 v[244:247], v[32:33], v[132:133], v[244:247]
	s_setprio 0
	s_barrier
	s_add_i32 s36, s36, 0x20000
	s_add_i32 s90, s90, 1
	s_cmpk_eq_i32 s90, 0x7e
	s_cbranch_scc1 .LBB0_305
	s_mov_b32 s14, s49
	s_mov_b32 s49, s51
	s_mov_b32 s51, s18
	s_mov_b32 s15, s50
	s_mov_b32 s50, s48
	s_mov_b32 s48, s37
	s_branch .LBB0_297
